# convert_in_tail (G2/G3 tails): wave-major row assignment so the 8192 table rows are spread evenly over the converting workgroups
# speedup vs baseline: 1.0276x; 1.0031x over previous
.LBB0_439:
	s_and_b64 vcc, exec, s[4:5]
	s_cbranch_vccz .LBB0_450
	s_ashr_i32 s37, s1, 6
	s_lshr_b32 s4, s0, 3
	s_mul_i32 s4, s4, s37
	s_lshr_b32 s27, s27, 3
	s_add_i32 s27, s27, s4
	s_mov_b32 s1, s27
	s_mov_b32 s37, 0
	s_nop 0
	s_cmpk_gt_i32 s1, 0x1fff
	s_cbranch_scc1 .LBB0_450
	s_lshl_b32 s4, s36, 14
	s_load_dwordx4 s[44:47], s[8:9], 0x80
	s_load_dwordx2 s[50:51], s[8:9], 0xa8
	s_add_i32 s6, s4, 0x6000
	s_add_i32 s4, s4, s1
	s_addk_i32 s4, 0x4000
	s_ashr_i32 s5, s4, 31
	s_lshl_b64 s[8:9], s[4:5], 13
	s_waitcnt vmcnt(0)
	v_and_b32_e32 v18, 63, v2
	s_waitcnt lgkmcnt(0)
	s_add_u32 s40, s44, s8
	s_addc_u32 s41, s45, s9
	v_lshlrev_b32_e32 v2, 5, v18
	v_lshl_add_u64 v[4:5], s[40:41], 0, v[2:3]
	v_add_co_u32_e32 v8, vcc, s77, v4
	s_add_u32 s8, s46, s8
	global_load_dwordx4 v[124:127], v2, s[40:41] offset:16 nt
	global_load_dwordx4 v[128:131], v2, s[40:41] nt
	global_load_dwordx4 v[116:119], v2, s[40:41] offset:2064 nt
	global_load_dwordx4 v[120:123], v2, s[40:41] offset:2048 nt
	s_mov_b64 s[40:41], 0x1000
	v_addc_co_u32_e32 v9, vcc, 0, v5, vcc
	s_mov_b64 s[42:43], 0x1800
	s_addc_u32 s9, s47, s9
	v_lshl_add_u64 v[6:7], v[4:5], 0, s[40:41]
	global_load_dwordx4 v[112:115], v[8:9], off nt
	global_load_dwordx4 v[108:111], v[6:7], off offset:16 nt
	v_lshl_add_u64 v[4:5], v[4:5], 0, s[42:43]
	global_load_dwordx4 v[104:107], v[8:9], off offset:2048 nt
	global_load_dwordx4 v[100:103], v[4:5], off offset:16 nt
	v_lshl_add_u64 v[8:9], s[8:9], 0, v[2:3]
	global_load_dwordx4 v[24:27], v2, s[8:9] offset:16 nt
	global_load_dwordx4 v[40:43], v2, s[8:9] nt
	global_load_dwordx4 v[4:7], v2, s[8:9] offset:2064 nt
	global_load_dwordx4 v[28:31], v2, s[8:9] offset:2048 nt
	v_add_co_u32_e32 v16, vcc, s77, v8
	v_lshl_add_u64 v[10:11], v[8:9], 0, s[40:41]
	s_nop 0
	v_addc_co_u32_e32 v17, vcc, 0, v9, vcc
	v_lshl_add_u64 v[8:9], v[8:9], 0, s[42:43]
	global_load_dwordx4 v[36:39], v[16:17], off nt
	global_load_dwordx4 v[12:15], v[10:11], off offset:16 nt
	global_load_dwordx4 v[32:35], v[16:17], off offset:2048 nt
	s_nop 0
	global_load_dwordx4 v[8:11], v[8:9], off offset:16 nt
	s_add_i32 s8, s1, s85
	s_ashr_i32 s9, s8, 31
	s_add_i32 s5, s27, s0
	s_lshl_b64 s[52:53], s[8:9], 3
	s_lshl_b64 s[8:9], s[8:9], 10
	s_add_i32 s5, s5, s37
	v_lshl_or_b32 v132, v18, 2, s8
	s_add_i32 s8, s5, s85
	s_ashr_i32 s1, s0, 31
	v_mov_b32_e32 v133, s9
	s_ashr_i32 s9, s8, 31
	s_lshl_b64 s[54:55], s[0:1], 3
	s_lshl_b64 s[56:57], s[0:1], 10
	s_lshl_b64 s[8:9], s[8:9], 13
	s_add_u32 s46, s46, s8
	s_addc_u32 s47, s47, s9
	s_lshl_b64 s[58:59], s[0:1], 13
	s_add_u32 s44, s44, s8
	v_cmp_eq_u32_e64 s[40:41], 0, v18
	s_addc_u32 s45, s45, s9
	s_branch .LBB0_443

.LBB0_614:
	s_and_b64 vcc, exec, s[4:5]
	s_cbranch_vccz .LBB0_625
	s_ashr_i32 s37, s1, 6
	s_lshr_b32 s4, s0, 3
	s_mul_i32 s4, s4, s37
	s_lshr_b32 s27, s27, 3
	s_add_i32 s27, s27, s4
	s_mov_b32 s1, s27
	s_mov_b32 s37, 0
	s_nop 0
	s_cmpk_gt_i32 s1, 0x1fff
	s_cbranch_scc1 .LBB0_625
	s_lshl_b32 s4, s36, 14
	s_load_dwordx4 s[44:47], s[8:9], 0x80
	s_load_dwordx2 s[48:49], s[8:9], 0xa8
	s_add_i32 s6, s4, 0x8000
	s_add_i32 s4, s4, s1
	s_addk_i32 s4, 0x6000
	s_ashr_i32 s5, s4, 31
	s_lshl_b64 s[8:9], s[4:5], 13
	s_waitcnt vmcnt(0)
	v_and_b32_e32 v18, 63, v2
	s_waitcnt lgkmcnt(0)
	s_add_u32 s40, s44, s8
	s_addc_u32 s41, s45, s9
	v_lshlrev_b32_e32 v2, 5, v18
	v_lshl_add_u64 v[4:5], s[40:41], 0, v[2:3]
	v_add_co_u32_e32 v8, vcc, s77, v4
	s_add_u32 s8, s46, s8
	global_load_dwordx4 v[124:127], v2, s[40:41] offset:16 nt
	global_load_dwordx4 v[128:131], v2, s[40:41] nt
	global_load_dwordx4 v[116:119], v2, s[40:41] offset:2064 nt
	global_load_dwordx4 v[120:123], v2, s[40:41] offset:2048 nt
	s_mov_b64 s[40:41], 0x1000
	v_addc_co_u32_e32 v9, vcc, 0, v5, vcc
	s_mov_b64 s[42:43], 0x1800
	s_addc_u32 s9, s47, s9
	v_lshl_add_u64 v[6:7], v[4:5], 0, s[40:41]
	global_load_dwordx4 v[112:115], v[8:9], off nt
	global_load_dwordx4 v[108:111], v[6:7], off offset:16 nt
	v_lshl_add_u64 v[4:5], v[4:5], 0, s[42:43]
	global_load_dwordx4 v[104:107], v[8:9], off offset:2048 nt
	global_load_dwordx4 v[100:103], v[4:5], off offset:16 nt
	v_lshl_add_u64 v[8:9], s[8:9], 0, v[2:3]
	global_load_dwordx4 v[24:27], v2, s[8:9] offset:16 nt
	global_load_dwordx4 v[40:43], v2, s[8:9] nt
	global_load_dwordx4 v[4:7], v2, s[8:9] offset:2064 nt
	global_load_dwordx4 v[28:31], v2, s[8:9] offset:2048 nt
	v_add_co_u32_e32 v16, vcc, s77, v8
	v_lshl_add_u64 v[10:11], v[8:9], 0, s[40:41]
	s_nop 0
	v_addc_co_u32_e32 v17, vcc, 0, v9, vcc
	v_lshl_add_u64 v[8:9], v[8:9], 0, s[42:43]
	global_load_dwordx4 v[36:39], v[16:17], off nt
	global_load_dwordx4 v[12:15], v[10:11], off offset:16 nt
	global_load_dwordx4 v[32:35], v[16:17], off offset:2048 nt
	s_nop 0
	global_load_dwordx4 v[8:11], v[8:9], off offset:16 nt
	v_readlane_b32 s42, v253, 12
	s_add_i32 s8, s1, s42
	s_ashr_i32 s9, s8, 31
	s_add_i32 s5, s27, s0
	s_lshl_b64 s[50:51], s[8:9], 3
	s_lshl_b64 s[8:9], s[8:9], 10
	s_add_i32 s5, s5, s37
	v_lshl_or_b32 v132, v18, 2, s8
	s_add_i32 s8, s5, s42
	s_ashr_i32 s1, s0, 31
	v_mov_b32_e32 v133, s9
	s_ashr_i32 s9, s8, 31
	s_lshl_b64 s[52:53], s[0:1], 3
	s_lshl_b64 s[54:55], s[0:1], 10
	s_lshl_b64 s[8:9], s[8:9], 13
	s_add_u32 s46, s46, s8
	s_addc_u32 s47, s47, s9
	s_lshl_b64 s[56:57], s[0:1], 13
	s_add_u32 s44, s44, s8
	v_cmp_eq_u32_e64 s[40:41], 0, v18
	s_addc_u32 s45, s45, s9
	s_branch .LBB0_618
